# P9/P12 workgroup start stagger widened (sleep steps 5 and 6 instead of 3 and 4)
# baseline (speedup 1.0000x reference)
.LBB0_1169:
.LBB0_1170:
	s_cmp_lt_i32 s26, 32
	s_cbranch_scc1 .Lstag9_done
	s_and_b32 s98, s26, 3
	s_mul_i32 s98, s98, 5
	s_cmp_eq_u32 s98, 0
	s_cbranch_scc1 .Lstag9_done

.LBB0_1589:
.LBB0_1590:
	s_cmp_lt_i32 s26, 32
	s_cbranch_scc1 .Lstag12_done
	s_and_b32 s98, s26, 3
	s_mul_i32 s98, s98, 6
	s_cmp_eq_u32 s98, 0
	s_cbranch_scc1 .Lstag12_done
